# baseline (speedup 1.0000x reference)
_Z11attn_kernelPKDF16_S0_S0_PfPDF16_S1_:
	s_lshl_b32 s3, s2, 7
	s_lshr_b32 s4, s2, 2
	s_and_b32 s3, s3, 0x180
	s_and_b32 s4, s4, 0x3ffffffe
	s_add_i32 s3, s3, s4
	s_bfe_u32 s2, s2, 0x10002
	s_or_b32 s40, s3, s2
	s_mov_b32 s41, 0
	s_lshl_b64 s[2:3], s[40:41], 2
	s_getpc_b64 s[4:5]
	s_add_u32 s4, s4, g_tab@rel32@lo+4
	s_addc_u32 s5, s5, g_tab@rel32@hi+12
	s_add_u32 s42, s4, s2
	s_addc_u32 s43, s5, s3
	s_load_dword s12, s[42:43], 0x0
	s_load_dwordx4 s[4:7], s[0:1], 0x8
	s_load_dword s76, s[42:43], 0x1000
	s_load_dwordx2 s[80:81], s[0:1], 0x0
	s_load_dwordx4 s[84:87], s[0:1], 0x18
	s_load_dwordx2 s[88:89], s[0:1], 0x28
	v_lshlrev_b32_e32 v2, 4, v0
	s_movk_i32 s8, 0x70
	v_readfirstlane_b32 s3, v0
	s_waitcnt lgkmcnt(0)
	s_add_u32 s70, s4, 0x2000
	s_addc_u32 s71, s5, 0
	s_add_u32 s72, s6, 0x2000
	s_addc_u32 s73, s7, 0
	s_and_b32 s2, s12, 3
	s_lshl_b32 s10, s2, 19
	v_bitop3_b32 v10, v2, s8, v0 bitop3:0x48
	s_add_u32 s8, s6, s10
	s_addc_u32 s9, s7, 0
	s_lshr_b32 s13, s3, 6
	s_bfe_u32 s40, s12, 0x70007
	s_bfe_u32 s33, s12, 0x6000e
	v_and_b32_e32 v1, 0x1f80, v2
	s_add_u32 s10, s4, s10
	v_or_b32_e32 v50, v10, v1
	v_mov_b32_e32 v51, 0
	s_addc_u32 s11, s5, 0
	v_lshl_add_u64 v[52:53], s[10:11], 0, v[50:51]
	v_lshl_add_u64 v[54:55], s[8:9], 0, v[50:51]
	s_lshl_b32 s8, s40, 13
	s_mov_b32 s9, s41
	s_lshl_b32 s50, s13, 10
	v_lshl_add_u64 v[2:3], v[52:53], 0, s[8:9]
	s_mov_b32 m0, s50
	s_add_i32 s51, s50, 0x2000
	global_load_lds_dwordx4 v[2:3], off
	v_lshl_add_u64 v[2:3], v[54:55], 0, s[8:9]
	s_mov_b32 m0, s51
	s_cmp_eq_u32 s33, 0
	global_load_lds_dwordx4 v[2:3], off
	s_cbranch_scc1 .LBB2_30
	s_mov_b64 s[14:15], s[80:81]
	s_mov_b64 s[8:9], s[84:85]
	s_mov_b64 s[10:11], s[86:87]
	s_mov_b64 s[44:45], s[88:89]
	s_lshl_b32 s52, s13, 4
	s_lshl_b32 s0, s2, 12
	v_and_b32_e32 v56, 15, v0
	v_bfe_u32 v15, v0, 4, 2
	v_lshrrev_b32_e32 v14, 1, v0
	v_bfe_u32 v2, v0, 1, 3
	s_add_i32 s54, s52, s0
	v_lshlrev_b32_e32 v16, 7, v56
	v_bitop3_b32 v3, v15, v14, 7 bitop3:0x78
	v_bitop3_b32 v2, v15, v2, 4 bitop3:0x36
	s_bfe_u32 s53, s12, 0x50002
	v_or_b32_e32 v18, s54, v56
	v_lshl_or_b32 v57, v3, 4, v16
	v_lshl_or_b32 v81, v2, 4, v16
	v_lshl_add_u32 v2, s53, 7, v18
	v_mov_b32_e32 v3, v51
	v_lshlrev_b64 v[2:3], 7, v[2:3]
	v_and_b32_e32 v50, 48, v0
	s_waitcnt lgkmcnt(0)
	v_lshl_add_u64 v[2:3], s[14:15], 0, v[2:3]
	v_lshl_add_u64 v[12:13], v[2:3], 0, v[50:51]
	global_load_dwordx4 v[2:5], v[12:13], off offset:64
	global_load_dwordx4 v[6:9], v[12:13], off
	v_and_b32_e32 v11, 63, v0
	v_bfe_u32 v12, v0, 5, 1
	s_mulk_i32 s13, 0xc00
	v_and_b32_e32 v13, 7, v0
	v_cmp_gt_u32_e64 s[0:1], 16, v11
	v_bitop3_b32 v11, v12, v0, 7 bitop3:0x78
	s_lshr_b32 s55, s3, 8
	s_add_i32 s3, s50, s13
	v_and_b32_e32 v14, 8, v14
	v_lshlrev_b32_e32 v23, 4, v11
	v_bitop3_b32 v11, v12, v13, 2 bitop3:0x36
	v_add3_u32 v19, s3, v16, v14
	v_bfe_u32 v14, v0, 3, 3
	v_lshlrev_b32_e32 v24, 4, v11
	v_bitop3_b32 v11, v12, v13, 4 bitop3:0x36
	v_bitop3_b32 v16, v14, v0, 7 bitop3:0x78
	v_lshlrev_b32_e32 v25, 4, v11
	v_bitop3_b32 v11, v12, v13, 6 bitop3:0x36
	v_bitop3_b32 v0, v15, v0, 15 bitop3:0x78
	v_lshl_add_u64 v[58:59], s[14:15], 0, v[50:51]
	v_lshlrev_b32_e32 v50, 4, v13
	v_lshlrev_b32_e32 v13, 4, v11
	v_or_b32_e32 v11, 8, v14
	v_lshlrev_b32_e32 v86, 4, v0
	v_bitop3_b32 v0, v15, v56, 4 bitop3:0x36
	v_or_b32_e32 v17, 4, v15
	v_lshl_add_u32 v21, v16, 4, s3
	v_lshlrev_b32_e32 v26, 7, v14
	v_lshlrev_b32_e32 v12, 6, v14
	v_lshlrev_b32_e32 v27, 7, v11
	v_lshlrev_b32_e32 v14, 6, v11
	v_lshlrev_b32_e32 v87, 4, v0
	v_or_b32_e32 v0, 8, v15
	v_bitop3_b32 v11, v15, v56, 8 bitop3:0x36
	v_bitop3_b32 v16, v15, v56, 12 bitop3:0x36
	v_lshlrev_b32_e32 v83, 2, v15
	v_add_u32_e32 v84, 0x80, v18
	v_lshl_add_u64 v[60:61], s[10:11], 0, v[50:51]
	v_lshlrev_b32_e32 v50, 4, v56
	v_lshlrev_b32_e32 v88, 4, v11
	v_or_b32_e32 v11, 12, v15
	v_lshlrev_b32_e32 v89, 4, v16
	v_lshl_add_u32 v28, v15, 8, s3
	v_lshlrev_b32_e32 v16, 6, v15
	v_lshl_add_u32 v15, v17, 8, s3
	v_lshlrev_b32_e32 v18, 6, v17
	v_lshl_add_u32 v17, v0, 8, s3
	v_lshlrev_b32_e32 v20, 6, v0
	v_add_u32_e32 v0, v1, v10
	v_lshl_add_u64 v[62:63], s[8:9], 0, v[50:51]
	s_lshl_b32 s8, s53, 1
	v_lshl_or_b32 v50, s2, 19, v0
	v_mov_b32_e32 v76, v50
	s_mov_b64 s[46:47], 0x2000
	v_lshl_add_u32 v85, v56, 8, s3
	v_lshl_add_u32 v29, v11, 8, s3
	v_lshlrev_b32_e32 v22, 6, v11
	s_add_i32 s3, s55, s8
	v_lshl_add_u64 v[10:11], v[50:51], 0, s[46:47]
	v_or_b32_e32 v82, s52, v56
	s_add_i32 s56, s8, 2
	s_sub_i32 s57, 0, s3
	v_lshl_add_u64 v[0:1], s[4:5], 0, v[10:11]
	v_lshl_add_u64 v[64:65], s[6:7], 0, v[10:11]
	s_mov_b32 s58, 0x40c00000
	s_mov_b32 s36, 0x3c003c00
	v_mov_b32_e32 v116, s36
	v_mov_b32_e32 v117, s36
	v_mov_b32_e32 v118, s36
	v_mov_b32_e32 v119, s36
	v_add_u32_e32 v90, v19, v23
	v_add_u32_e32 v91, v19, v24
	v_add_u32_e32 v92, v19, v25
	v_add_u32_e32 v93, v19, v13
	v_add_u32_e32 v94, v21, v26
	v_lshlrev_b32_e32 v50, 1, v12
	v_add_u32_e32 v95, v21, v27
	v_lshlrev_b32_e32 v66, 1, v14
	v_add_u32_e32 v96, v28, v86
	v_lshlrev_b32_e32 v68, 2, v16
	v_add_u32_e32 v97, v15, v87
	v_lshlrev_b32_e32 v70, 2, v18
	v_add_u32_e32 v98, v17, v88
	v_lshlrev_b32_e32 v72, 2, v20
	v_add_u32_e32 v99, v29, v89
	v_lshlrev_b32_e32 v74, 2, v22
	v_mov_b32_e32 v100, 0xff800000
	v_mov_b32_e32 v101, 0xf149f2ca
	s_mov_b32 s59, s41
	s_branch .LBB2_3

.LBB2_24:
	s_cmp_lg_u32 s40, 0
	s_cselect_b64 s[4:5], -1, 0
	s_cmp_lg_u32 s62, s61
	s_cselect_b64 s[6:7], -1, 0
	s_or_b64 s[6:7], s[4:5], s[6:7]
	s_mov_b64 s[4:5], -1
	s_and_b64 vcc, exec, s[6:7]
	s_cbranch_vccz .LBB2_28
	v_div_scale_f32 v15, s[4:5], v14, v14, 1.0
	v_rcp_f32_e32 v17, v15
	v_mov_b32_e32 v33, v28
	v_mov_b32_e32 v67, v51
	v_fma_f32 v30, -v15, v17, 1.0
	v_fmac_f32_e32 v17, v30, v17
	v_div_scale_f32 v30, vcc, 1.0, v14, 1.0
	v_mul_f32_e32 v31, v30, v17
	v_fma_f32 v32, -v15, v31, v30
	v_fmac_f32_e32 v31, v32, v17
	v_fma_f32 v15, -v15, v31, v30
	v_div_fmas_f32 v15, v15, v17, v31
	v_div_fixup_f32 v15, v15, v14, 1.0
	v_cmp_lt_f32_e32 vcc, 0, v14
	v_mov_b32_e32 v32, v27
	s_add_i32 s4, s76, s59
	v_cndmask_b32_e32 v30, 0, v15, vcc
	v_pk_mul_f32 v[32:33], v[30:31], v[32:33] op_sel_hi:[0,1]
	v_fma_mixlo_f16 v15, v30, v26, 0
	v_cvt_pk_f16_f32 v17, v32, v33
	v_pack_b32_f16 v32, v15, v17
	v_fma_mixlo_f16 v15, v30, v29, 0
	v_alignbit_b32 v33, v15, v17, 16
	ds_write_b64 v90, v[32:33] offset:32768
	v_mov_b32_e32 v32, v23
	v_mov_b32_e32 v33, v24
	v_pk_mul_f32 v[32:33], v[30:31], v[32:33] op_sel_hi:[0,1]
	v_fma_mixlo_f16 v15, v30, v22, 0
	v_cvt_pk_f16_f32 v17, v32, v33
	v_pack_b32_f16 v32, v15, v17
	v_fma_mixlo_f16 v15, v30, v25, 0
	v_alignbit_b32 v33, v15, v17, 16
	ds_write_b64 v91, v[32:33] offset:32768
	v_mov_b32_e32 v32, v19
	v_mov_b32_e32 v33, v20
	v_pk_mul_f32 v[32:33], v[30:31], v[32:33] op_sel_hi:[0,1]
	v_fma_mixlo_f16 v15, v30, v18, 0
	v_cvt_pk_f16_f32 v17, v32, v33
	v_pack_b32_f16 v32, v15, v17
	v_fma_mixlo_f16 v15, v30, v21, 0
	v_alignbit_b32 v33, v15, v17, 16
	ds_write_b64 v92, v[32:33] offset:32768
	v_mov_b32_e32 v32, v11
	v_mov_b32_e32 v33, v12
	v_pk_mul_f32 v[32:33], v[30:31], v[32:33] op_sel_hi:[0,1]
	v_fma_mixlo_f16 v15, v30, v10, 0
	v_cvt_pk_f16_f32 v17, v32, v33
	v_pack_b32_f16 v32, v15, v17
	v_fma_mixlo_f16 v15, v30, v13, 0
	v_alignbit_b32 v33, v15, v17, 16
	s_ashr_i32 s5, s4, 31
	ds_write_b64 v93, v[32:33] offset:32768
	s_lshl_b64 s[4:5], s[4:5], 7
	s_add_u32 s4, s4, s52
	s_waitcnt vmcnt(0)
	ds_read_b128 v[30:33], v94 offset:32768
	ds_read_b128 v[34:37], v95 offset:32768
	s_addc_u32 s5, s5, 0
	s_lshl_b64 s[6:7], s[4:5], 7
	v_lshl_add_u64 v[38:39], v[60:61], 0, s[6:7]
	v_lshl_add_u64 v[40:41], v[38:39], 0, v[50:51]
	s_waitcnt lgkmcnt(1)
	global_store_dwordx4 v[40:41], v[30:33], off sc1
	s_nop 1
	v_lshl_add_u64 v[30:31], v[38:39], 0, v[66:67]
	s_waitcnt lgkmcnt(0)
	global_store_dwordx4 v[30:31], v[34:37], off sc1
	s_and_saveexec_b64 s[6:7], s[0:1]
	s_cbranch_execz .LBB2_27
	v_mov_b32_e32 v31, s5
	v_or_b32_e32 v30, s4, v56
	v_lshl_add_u64 v[30:31], v[30:31], 3, s[44:45]
	v_mov_b32_e32 v17, v14
	global_store_dwordx2 v[30:31], v[16:17], off sc1

amdhsa.kernels:
  - .agpr_count:     0
    .args:
      - .actual_access:  read_only
        .address_space:  global
        .offset:         0
        .size:           8
        .value_kind:     global_buffer
      - .actual_access:  read_only
        .address_space:  global
        .offset:         8
        .size:           8
        .value_kind:     global_buffer
      - .actual_access:  read_only
        .address_space:  global
        .offset:         16
        .size:           8
        .value_kind:     global_buffer
      - .actual_access:  write_only
        .address_space:  global
        .offset:         24
        .size:           8
        .value_kind:     global_buffer
      - .offset:         32
        .size:           4
        .value_kind:     hidden_block_count_x
      - .offset:         36
        .size:           4
        .value_kind:     hidden_block_count_y
      - .offset:         40
        .size:           4
        .value_kind:     hidden_block_count_z
      - .offset:         44
        .size:           2
        .value_kind:     hidden_group_size_x
      - .offset:         46
        .size:           2
        .value_kind:     hidden_group_size_y
      - .offset:         48
        .size:           2
        .value_kind:     hidden_group_size_z
      - .offset:         50
        .size:           2
        .value_kind:     hidden_remainder_x
      - .offset:         52
        .size:           2
        .value_kind:     hidden_remainder_y
      - .offset:         54
        .size:           2
        .value_kind:     hidden_remainder_z
      - .offset:         72
        .size:           8
        .value_kind:     hidden_global_offset_x
      - .offset:         80
        .size:           8
        .value_kind:     hidden_global_offset_y
      - .offset:         88
        .size:           8
        .value_kind:     hidden_global_offset_z
      - .offset:         96
        .size:           2
        .value_kind:     hidden_grid_dims
    .group_segment_fixed_size: 0
    .kernarg_segment_align: 8
    .kernarg_segment_size: 288
    .language:       OpenCL C
    .language_version:
      - 2
      - 0
    .max_flat_workgroup_size: 1024
    .name:           _Z13prep_w_kernelPKfS0_S0_PDv8_DF16_
    .private_segment_fixed_size: 0
    .sgpr_count:     18
    .sgpr_spill_count: 0
    .symbol:         _Z13prep_w_kernelPKfS0_S0_PDv8_DF16_.kd
    .uniform_work_group_size: 1
    .uses_dynamic_stack: false
    .vgpr_count:     15
    .vgpr_spill_count: 0
    .wavefront_size: 64
  - .agpr_count:     0
    .args:
      - .actual_access:  read_only
        .address_space:  global
        .offset:         0
        .size:           8
        .value_kind:     global_buffer
      - .actual_access:  read_only
        .address_space:  global
        .offset:         8
        .size:           8
        .value_kind:     global_buffer
      - .actual_access:  write_only
        .address_space:  global
        .offset:         16
        .size:           8
        .value_kind:     global_buffer
      - .actual_access:  write_only
        .address_space:  global
        .offset:         24
        .size:           8
        .value_kind:     global_buffer
      - .actual_access:  write_only
        .address_space:  global
        .offset:         32
        .size:           8
        .value_kind:     global_buffer
    .group_segment_fixed_size: 131328
    .kernarg_segment_align: 8
    .kernarg_segment_size: 40
    .language:       OpenCL C
    .language_version:
      - 2
      - 0
    .max_flat_workgroup_size: 512
    .name:           _Z11proj_kernelPKfPKDv8_DF16_PDF16_S4_S4_
    .private_segment_fixed_size: 0
    .sgpr_count:     26
    .sgpr_spill_count: 0
    .symbol:         _Z11proj_kernelPKfPKDv8_DF16_PDF16_S4_S4_.kd
    .uniform_work_group_size: 1
    .uses_dynamic_stack: false
    .vgpr_count:     176
    .vgpr_spill_count: 0
    .wavefront_size: 64
  - .agpr_count:     0
    .args:
      - .actual_access:  read_only
        .address_space:  global
        .offset:         0
        .size:           8
        .value_kind:     global_buffer
      - .address_space:  global
        .offset:         8
        .size:           8
        .value_kind:     global_buffer
      - .address_space:  global
        .offset:         16
        .size:           8
        .value_kind:     global_buffer
      - .actual_access:  write_only
        .address_space:  global
        .offset:         24
        .size:           8
        .value_kind:     global_buffer
      - .actual_access:  write_only
        .address_space:  global
        .offset:         32
        .size:           8
        .value_kind:     global_buffer
      - .actual_access:  write_only
        .address_space:  global
        .offset:         40
        .size:           8
        .value_kind:     global_buffer
    .group_segment_fixed_size: 65536
    .kernarg_segment_align: 8
    .kernarg_segment_size: 48
    .language:       OpenCL C
    .language_version:
      - 2
      - 0
    .max_flat_workgroup_size: 512
    .name:           _Z11attn_kernelPKDF16_S0_S0_PfPDF16_S1_
    .private_segment_fixed_size: 0
    .sgpr_count:     96
    .sgpr_spill_count: 0
    .symbol:         _Z11attn_kernelPKDF16_S0_S0_PfPDF16_S1_.kd
    .uniform_work_group_size: 1
    .uses_dynamic_stack: false
    .vgpr_count:     120
    .vgpr_spill_count: 0
    .wavefront_size: 64
  - .agpr_count:     0
    .args:
      - .actual_access:  read_only
        .address_space:  global
        .offset:         0
        .size:           8
        .value_kind:     global_buffer
      - .actual_access:  read_only
        .address_space:  global
        .offset:         8
        .size:           8
        .value_kind:     global_buffer
      - .actual_access:  write_only
        .address_space:  global
        .offset:         16
        .size:           8
        .value_kind:     global_buffer
    .group_segment_fixed_size: 0
    .kernarg_segment_align: 8
    .kernarg_segment_size: 24
    .language:       OpenCL C
    .language_version:
      - 2
      - 0
    .max_flat_workgroup_size: 256
    .name:           _Z14combine_kernelPKDF16_PKfPf
    .private_segment_fixed_size: 0
    .sgpr_count:     70
    .sgpr_spill_count: 0
    .symbol:         _Z14combine_kernelPKDF16_PKfPf.kd
    .uniform_work_group_size: 1
    .uses_dynamic_stack: false
    .vgpr_count:     46
    .vgpr_spill_count: 0
    .wavefront_size: 64
